# P8: next chunk's D7 row loaded one chunk ahead beside the x prefetch; moe_norm gain quads kept 5 deep in flight (rolling) instead of one load behind each store
# baseline (speedup 1.0000x reference)
; #define LAS __attribute__((address_space(3)))
; __global__ void __launch_bounds__(512, 2) mega_fwd(Args args) {
;     ...
;         constexpr int AST = 4112;
;         LAS unsigned char* Ahi = lds; LAS unsigned char* Alo = lds + 16 * AST; LAS float* part = (LAS float*)(lds + 32 * AST);
;         const float* gn = args.in[I_MOE_NORM]; const float* br = args.in[I_B_ROUTER];
;         const bf16_t* WRH = (const bf16_t*)(ws + WS_WRH); const bf16_t* WRL = (const bf16_t*)(ws + WS_WRL);
;         bf16x8 bh[2][8], bl[2][8];
; #pragma unroll
;         for (int nt = 0; nt < 2; ++nt)
; #pragma unroll
;             for (int ks = 0; ks < 8; ++ks) { const size_t o = (size_t)(nt * 16 + (lane & 15)) * DM + wave * 256 + ks * 32 + (lane >> 4) * 8; bh[nt][ks] = *(const bf16x8*)(WRH + o); bl[nt][ks] = *(const bf16x8*)(WRL + o); }
.LBB0_1992:
	s_cmp_lt_i32 s20, 9
	s_cselect_b64 s[6:7], -1, 0
	s_lshl_b32 s3, s2, 3
	s_add_i32 s38, s74, s3
	s_lshl_b32 s40, s82, 3
	s_add_u32 s42, s18, 0x400000
	s_addc_u32 s43, s19, 0
	s_add_u32 s44, s18, 0x500000
	s_addc_u32 s45, s19, 0
	s_add_u32 s46, s18, 0x600000
	s_addc_u32 s47, s19, 0
	s_add_u32 s48, s18, 0x2f000000
	s_addc_u32 s49, s19, 0
	s_and_b64 s[6:7], s[6:7], s[8:9]
	s_andn2_b64 vcc, exec, s[6:7]
	s_cbranch_vccnz .LBB0_2290
	s_cmpk_gt_i32 s2, 0x7ff
	s_cbranch_scc1 .LBB0_2001
	v_lshlrev_b32_e32 v1, 11, v0
	s_waitcnt vmcnt(15)
	v_lshrrev_b32_e32 v2, 1, v0
	s_movk_i32 s10, 0x7818
	s_add_u32 s6, s18, 0x280000
	v_bitop3_b32 v1, v2, s10, v1 bitop3:0xc8
	s_addc_u32 s7, s19, 0
	v_lshl_add_u32 v188, s74, 8, v1
	v_mov_b32_e32 v189, 0
	s_add_u32 s8, s18, 0x2c0000
	v_lshlrev_b64 v[2:3], 1, v[188:189]
	s_waitcnt vmcnt(13) lgkmcnt(1)
	v_or_b32_e32 v10, 32, v188
	s_waitcnt lgkmcnt(0)
	v_mov_b32_e32 v11, v189
	s_waitcnt vmcnt(2)
	v_or_b32_e32 v18, 64, v188
	v_mov_b32_e32 v19, v189
	s_waitcnt vmcnt(0)
	v_or_b32_e32 v26, 0x60, v188
	v_mov_b32_e32 v27, v189
	v_or_b32_e32 v34, 0x80, v188
	v_mov_b32_e32 v35, v189
	v_or_b32_e32 v42, 0xa0, v188
	v_mov_b32_e32 v43, v189
	v_or_b32_e32 v50, 0xc0, v188
	v_mov_b32_e32 v51, v189
	v_or_b32_e32 v58, 0xe0, v188
	v_mov_b32_e32 v59, v189
	v_add_u32_e32 v66, 0x8000, v188
	v_mov_b32_e32 v67, v189
	v_add_u32_e32 v74, 0x8020, v188
	v_mov_b32_e32 v75, v189
	v_add_u32_e32 v82, 0x8040, v188
	v_mov_b32_e32 v83, v189
	v_add_u32_e32 v90, 0x8060, v188
	v_mov_b32_e32 v91, v189
	v_add_u32_e32 v98, 0x8080, v188
	v_mov_b32_e32 v99, v189
	v_add_u32_e32 v106, 0x80a0, v188
	v_mov_b32_e32 v107, v189
	v_add_u32_e32 v114, 0x80c0, v188
	v_mov_b32_e32 v115, v189
	v_add_u32_e32 v188, 0x80e0, v188
	s_addc_u32 s9, s19, 0
	v_lshlrev_b64 v[10:11], 1, v[10:11]
	v_lshlrev_b64 v[18:19], 1, v[18:19]
	v_lshlrev_b64 v[26:27], 1, v[26:27]
	v_lshlrev_b64 v[34:35], 1, v[34:35]
	v_lshlrev_b64 v[42:43], 1, v[42:43]
	v_lshlrev_b64 v[50:51], 1, v[50:51]
	v_lshlrev_b64 v[58:59], 1, v[58:59]
	v_lshlrev_b64 v[66:67], 1, v[66:67]
	v_lshlrev_b64 v[74:75], 1, v[74:75]
	v_lshlrev_b64 v[82:83], 1, v[82:83]
	v_lshlrev_b64 v[90:91], 1, v[90:91]
	v_lshlrev_b64 v[98:99], 1, v[98:99]
	v_lshlrev_b64 v[106:107], 1, v[106:107]
	v_lshlrev_b64 v[114:115], 1, v[114:115]
	v_lshlrev_b64 v[122:123], 1, v[188:189]
	v_lshl_add_u64 v[6:7], s[8:9], 0, v[2:3]
	v_lshl_add_u64 v[14:15], s[8:9], 0, v[10:11]
	v_lshl_add_u64 v[22:23], s[8:9], 0, v[18:19]
	v_lshl_add_u64 v[30:31], s[8:9], 0, v[26:27]
	v_lshl_add_u64 v[38:39], s[8:9], 0, v[34:35]
	v_lshl_add_u64 v[46:47], s[8:9], 0, v[42:43]
	v_lshl_add_u64 v[54:55], s[8:9], 0, v[50:51]
	v_lshl_add_u64 v[62:63], s[8:9], 0, v[58:59]
	v_lshl_add_u64 v[70:71], s[8:9], 0, v[66:67]
	v_lshl_add_u64 v[78:79], s[8:9], 0, v[74:75]
	v_lshl_add_u64 v[86:87], s[8:9], 0, v[82:83]
	v_lshl_add_u64 v[94:95], s[8:9], 0, v[90:91]
	v_lshl_add_u64 v[102:103], s[8:9], 0, v[98:99]
	v_lshl_add_u64 v[110:111], s[8:9], 0, v[106:107]
	v_lshl_add_u64 v[118:119], s[8:9], 0, v[114:115]
	v_lshl_add_u64 v[126:127], s[8:9], 0, v[122:123]
	s_load_dwordx2 s[8:9], s[0:1], 0x0
	s_ashr_i32 s39, s38, 31
	v_lshl_add_u64 v[4:5], s[6:7], 0, v[2:3]
	v_lshl_add_u64 v[12:13], s[6:7], 0, v[10:11]
	v_lshl_add_u64 v[20:21], s[6:7], 0, v[18:19]
	v_lshl_add_u64 v[28:29], s[6:7], 0, v[26:27]
	v_lshl_add_u64 v[36:37], s[6:7], 0, v[34:35]
	v_lshl_add_u64 v[44:45], s[6:7], 0, v[42:43]
	v_lshl_add_u64 v[52:53], s[6:7], 0, v[50:51]
	v_lshl_add_u64 v[60:61], s[6:7], 0, v[58:59]
	v_lshl_add_u64 v[68:69], s[6:7], 0, v[66:67]
	v_lshl_add_u64 v[76:77], s[6:7], 0, v[74:75]
	v_lshl_add_u64 v[84:85], s[6:7], 0, v[82:83]
	v_lshl_add_u64 v[92:93], s[6:7], 0, v[90:91]
	v_lshl_add_u64 v[100:101], s[6:7], 0, v[98:99]
	v_lshl_add_u64 v[108:109], s[6:7], 0, v[106:107]
	v_lshl_add_u64 v[116:117], s[6:7], 0, v[114:115]
	v_lshl_add_u64 v[124:125], s[6:7], 0, v[122:123]
	s_lshl_b64 s[6:7], s[38:39], 13
	s_waitcnt lgkmcnt(0)
; __global__ void __launch_bounds__(512, 2) mega_fwd(Args args) {
;     ...
;         constexpr int RPW = 1, CR = 8 * RPW;
;         f32x4 nv[RPW][8];
;         int ch = bx;
;         if (ch < T / CR) {
; #pragma unroll
;             for (int r = 0; r < RPW; ++r) { const f32x4* xr = (const f32x4*)(x + (size_t)(ch * CR + wave * RPW + r) * DM) + lane;
; #pragma unroll
;                 for (int j = 0; j < 8; ++j) nv[r][j] = xr[64 * j]; } }
;         for (; ch < T / CR; ch += G) {
; #pragma unroll
;             for (int r = 0; r < RPW; ++r) { const int rowc = wave * RPW + r, m = ch * CR + rowc; float ssq = 0.f;
;                 { const u32x2* dr = (const u32x2*)(D7 + (size_t)m * DM) + lane; u32x2* hr = (u32x2*)(H1 + (size_t)m * DM) + lane;
	s_add_u32 s6, s8, s6
	s_addc_u32 s7, s9, s7
	v_lshlrev_b32_e32 v188, 4, v164
	global_load_dwordx4 v[2:5], v[4:5], off
	s_nop 0
	global_load_dwordx4 v[6:9], v[6:7], off
	s_nop 0
	global_load_dwordx4 v[10:13], v[12:13], off
	s_nop 0
	global_load_dwordx4 v[14:17], v[14:15], off
	s_nop 0
	global_load_dwordx4 v[18:21], v[20:21], off
	s_nop 0
	global_load_dwordx4 v[22:25], v[22:23], off
	s_nop 0
	global_load_dwordx4 v[26:29], v[28:29], off
	s_nop 0
	global_load_dwordx4 v[30:33], v[30:31], off
	s_nop 0
	global_load_dwordx4 v[34:37], v[36:37], off
	s_nop 0
	global_load_dwordx4 v[38:41], v[38:39], off
	s_nop 0
	global_load_dwordx4 v[42:45], v[44:45], off
	s_nop 0
	global_load_dwordx4 v[46:49], v[46:47], off
	s_nop 0
	global_load_dwordx4 v[50:53], v[52:53], off
	s_nop 0
	global_load_dwordx4 v[54:57], v[54:55], off
	s_nop 0
	global_load_dwordx4 v[58:61], v[60:61], off
	s_nop 0
	global_load_dwordx4 v[62:65], v[62:63], off
	s_nop 0
	global_load_dwordx4 v[66:69], v[68:69], off
	s_nop 0
	global_load_dwordx4 v[70:73], v[70:71], off
	s_nop 0
	global_load_dwordx4 v[74:77], v[76:77], off
	s_nop 0
	global_load_dwordx4 v[78:81], v[78:79], off
	s_nop 0
	global_load_dwordx4 v[82:85], v[84:85], off
	s_nop 0
	global_load_dwordx4 v[86:89], v[86:87], off
	s_nop 0
	global_load_dwordx4 v[90:93], v[92:93], off
	s_nop 0
	global_load_dwordx4 v[94:97], v[94:95], off
	s_nop 0
	global_load_dwordx4 v[98:101], v[100:101], off
	s_nop 0
	global_load_dwordx4 v[102:105], v[102:103], off
	s_nop 0
	global_load_dwordx4 v[106:109], v[108:109], off
	s_nop 0
	global_load_dwordx4 v[110:113], v[110:111], off
	s_nop 0
	global_load_dwordx4 v[114:117], v[116:117], off
	s_nop 0
	global_load_dwordx4 v[118:121], v[118:119], off
	s_nop 0
	global_load_dwordx4 v[122:125], v[124:125], off
	s_nop 0
	global_load_dwordx4 v[126:129], v[126:127], off
	v_lshl_add_u64 v[146:147], s[6:7], 0, v[188:189]
	global_load_dwordx4 v[130:133], v188, s[6:7]
	global_load_dwordx4 v[134:137], v188, s[6:7] offset:1024
	global_load_dwordx4 v[138:141], v188, s[6:7] offset:2048
	global_load_dwordx4 v[142:145], v188, s[6:7] offset:3072
	s_movk_i32 s6, 0x1000
	v_add_co_u32_e32 v158, vcc, s6, v146
	v_lshlrev_b32_e32 v162, 3, v164
	s_nop 0
	v_addc_co_u32_e32 v159, vcc, 0, v147, vcc
	global_load_dwordx4 v[146:149], v[158:159], off
	global_load_dwordx4 v[150:153], v[158:159], off offset:1024
	global_load_dwordx4 v[154:157], v[158:159], off offset:2048
	s_nop 0
	global_load_dwordx4 v[158:161], v[158:159], off offset:3072
	s_load_dwordx2 s[16:17], s[0:1], 0x60
	s_load_dwordx2 s[6:7], s[0:1], 0x70
	v_mov_b32_e32 v163, v189
	v_or_b32_e32 v184, 0x100, v164
	v_lshl_add_u64 v[168:169], s[4:5], 0, v[162:163]
	v_lshl_add_u64 v[170:171], s[18:19], 0, v[162:163]
	s_mov_b64 s[4:5], 0x1d000000
	v_lshl_add_u64 v[174:175], s[8:9], 0, v[188:189]
	s_waitcnt lgkmcnt(0)
	v_lshl_add_u64 v[180:181], s[16:17], 0, v[188:189]
	v_lshlrev_b32_e32 v188, 4, v184
	v_or_b32_e32 v186, 0x140, v164
	v_lshl_add_u64 v[170:171], v[170:171], 0, s[4:5]
	s_mul_i32 s4, s74, 0x1010
	v_lshl_add_u64 v[182:183], s[16:17], 0, v[188:189]
	v_lshlrev_b32_e32 v188, 4, v186
	v_or_b32_e32 v190, 0x180, v164
	s_add_i32 s26, s4, 0
	v_and_b32_e32 v1, 15, v0
	v_lshlrev_b32_e32 v197, 3, v184
	v_lshl_add_u64 v[184:185], s[16:17], 0, v[188:189]
	v_lshlrev_b32_e32 v188, 4, v190
	v_lshlrev_b32_e32 v199, 3, v190
	v_or_b32_e32 v190, 0x1c0, v164
	s_add_i32 s27, s26, 0x10100
	v_mul_u32_u24_e32 v163, 0x1010, v1
	s_lshl_b32 s4, s74, 9
	v_and_b32_e32 v165, 48, v0
	s_add_i32 s8, 0, 0x20200
	v_lshlrev_b32_e32 v198, 3, v186
	v_lshl_add_u64 v[186:187], s[16:17], 0, v[188:189]
	v_lshlrev_b32_e32 v188, 4, v190
	v_lshlrev_b32_e32 v200, 3, v190
	v_lshlrev_b32_e32 v190, 5, v0
	v_add3_u32 v191, v163, v165, s4
	v_lshl_add_u32 v192, v1, 2, s8
	v_lshrrev_b32_e32 v1, 5, v0
	v_and_b32_e32 v163, 31, v0
	v_and_b32_e32 v165, 0xe0, v0
	s_add_u32 s50, s18, 0x10000
	v_and_b32_e32 v190, 0x600, v190
	v_lshlrev_b32_e32 v172, 2, v164
	v_mov_b32_e32 v173, v189
	s_movk_i32 s4, 0x100
	v_lshlrev_b32_e32 v178, 2, v163
	v_mov_b32_e32 v179, v189
	v_lshlrev_b32_e32 v165, 2, v165
	s_addc_u32 s51, s19, 0
	v_lshl_add_u64 v[188:189], s[16:17], 0, v[188:189]
	v_lshl_or_b32 v193, s74, 11, v190
	s_lshl_b32 s16, s2, 5
	v_lshlrev_b32_e32 v190, 2, v1
	v_add_u32_e32 v203, 0, v191
	v_mbcnt_lo_u32_b32 v191, -1, 0
	v_lshl_add_u64 v[172:173], s[24:25], 0, v[172:173]
	v_cmp_gt_u32_e64 s[4:5], s4, v0
	v_lshl_add_u64 v[176:177], s[6:7], 0, v[178:179]
	v_add3_u32 v165, s8, v165, v178
	v_and_b32_e32 v178, 32, v0
	v_cmp_gt_u32_e64 s[6:7], 4, v163
	v_cmp_eq_u32_e64 s[8:9], 0, v163
	v_cmp_eq_u32_e64 s[10:11], 1, v163
	v_cmp_eq_u32_e64 s[12:13], 2, v163
	v_or_b32_e32 v167, 0x200, v162
	v_or_b32_e32 v179, 0x400, v162
	v_or_b32_e32 v196, 0x600, v162
	v_add3_u32 v190, s16, v190, v163
	s_lshl_b32 s39, s82, 5
	s_add_i32 s41, s74, s40
	v_mov_b32_e32 v201, 0x358637bd
	s_mov_b32 s54, 0xf800000
	v_mov_b32_e32 v202, 0x260
	v_add_u32_e32 v204, v192, v193
	v_mov_b32_e32 v205, 1
	v_mbcnt_hi_u32_b32 v206, -1, v191
	v_mov_b32_e32 v207, 0xff800000
	s_mov_b32 s55, s2
	s_add_i32 s98, s74, s3
	s_ashr_i32 s99, s98, 31
	s_lshl_b64 s[98:99], s[98:99], 12
	v_lshl_add_u64 v[248:249], v[168:169], 0, s[98:99]
	global_load_dwordx2 v[232:233], v[248:249], off
	global_load_dwordx2 v[234:235], v[248:249], off offset:512
	global_load_dwordx2 v[236:237], v[248:249], off offset:1024
	global_load_dwordx2 v[238:239], v[248:249], off offset:1536
	global_load_dwordx2 v[240:241], v[248:249], off offset:2048
	global_load_dwordx2 v[242:243], v[248:249], off offset:2560
	global_load_dwordx2 v[244:245], v[248:249], off offset:3072
	global_load_dwordx2 v[246:247], v[248:249], off offset:3584
	s_branch .LBB0_1996

; __device__ __forceinline__ unsigned cvtpk(float lo, float hi) { unsigned r; asm volatile("v_cvt_pk_bf16_f32 %0, %1, %2" : "=v"(r) : "v"(lo), "v"(hi)); return r; }
; __device__ __forceinline__ float bflo(unsigned w) { return __uint_as_float(w << 16); }
; __device__ __forceinline__ float bfhi(unsigned w) { return __uint_as_float(w & 0xffff0000u); }
; __global__ void __launch_bounds__(512, 2) mega_fwd(Args args) {
;     ...
;             for (int r = 0; r < RPW; ++r) { const int rowc = wave * RPW + r, m = ch * CR + rowc; float ssq = 0.f;
;                 { const u32x2* dr = (const u32x2*)(D7 + (size_t)m * DM) + lane; u32x2* hr = (u32x2*)(H1 + (size_t)m * DM) + lane;
; #pragma unroll
;                   for (int j = 0; j < 8; ++j) { const u32x2 d = dr[64 * j]; nv[r][j][0] += bflo(d.x); nv[r][j][1] += bfhi(d.x); nv[r][j][2] += bflo(d.y); nv[r][j][3] += bfhi(d.y); u32x2 hw_; hw_.x = cvtpk(nv[r][j][0], nv[r][j][1]); hw_.y = cvtpk(nv[r][j][2], nv[r][j][3]); hr[64 * j] = hw_; } }
; #pragma unroll
;                 for (int j = 0; j < 8; ++j) ssq += (nv[r][j][0] * nv[r][j][0] + nv[r][j][1] * nv[r][j][1]) + (nv[r][j][2] * nv[r][j][2] + nv[r][j][3] * nv[r][j][3]);
.LBB0_1996:
	s_add_i32 s52, s74, s3
	s_ashr_i32 s53, s52, 31
	s_lshl_b64 s[16:17], s[52:53], 12
	v_lshl_add_u64 v[194:195], v[168:169], 0, s[16:17]
	v_and_b32_e32 v191, 64, v206
	v_add_u32_e32 v224, 64, v191
	s_add_i32 s55, s55, s82
	v_add_u32_e32 v225, s27, v200
	s_waitcnt vmcnt(7)
	v_mov_b32_e32 v192, v232
	v_mov_b32_e32 v193, v233
	v_lshlrev_b32_e32 v208, 16, v192
	v_and_b32_e32 v209, 0xffff0000, v192
	v_lshlrev_b32_e32 v192, 16, v193
	v_and_b32_e32 v193, 0xffff0000, v193
	v_pk_add_f32 v[130:131], v[130:131], v[208:209]
	v_pk_add_f32 v[132:133], v[132:133], v[192:193]
	v_cvt_pk_bf16_f32 v208, v130, v131
	v_lshl_add_u64 v[192:193], v[170:171], 0, s[16:17]
	v_cvt_pk_bf16_f32 v209, v132, v133
	v_mov_b32_e32 v212, v131
	global_store_dwordx2 v[192:193], v[208:209], off
	v_mov_b32_e32 v216, v133
	v_mov_b32_e32 v214, v132
	s_waitcnt vmcnt(7)
	v_mov_b32_e32 v210, v234
	v_mov_b32_e32 v211, v235
	v_lshlrev_b32_e32 v208, 16, v210
	v_and_b32_e32 v209, 0xffff0000, v210
	v_lshlrev_b32_e32 v210, 16, v211
	v_and_b32_e32 v211, 0xffff0000, v211
	v_pk_add_f32 v[134:135], v[134:135], v[208:209]
	v_pk_add_f32 v[136:137], v[136:137], v[210:211]
	v_cvt_pk_bf16_f32 v208, v134, v135
	v_mov_b32_e32 v213, v135
	v_cvt_pk_bf16_f32 v209, v136, v137
	v_mov_b32_e32 v217, v137
	global_store_dwordx2 v[192:193], v[208:209], off offset:512
	v_mov_b32_e32 v215, v136
	v_pk_mul_f32 v[212:213], v[212:213], v[212:213]
	v_pk_mul_f32 v[216:217], v[216:217], v[216:217]
	s_waitcnt vmcnt(7)
	v_mov_b32_e32 v210, v236
	v_mov_b32_e32 v211, v237
	v_lshlrev_b32_e32 v208, 16, v210
	v_and_b32_e32 v209, 0xffff0000, v210
	v_lshlrev_b32_e32 v210, 16, v211
	v_and_b32_e32 v211, 0xffff0000, v211
	v_pk_add_f32 v[138:139], v[138:139], v[208:209]
	v_pk_add_f32 v[140:141], v[140:141], v[210:211]
	v_cvt_pk_bf16_f32 v208, v138, v139
	s_nop 0
	v_cvt_pk_bf16_f32 v209, v140, v141
	s_nop 0
	global_store_dwordx2 v[192:193], v[208:209], off offset:1024
	s_waitcnt vmcnt(7)
	v_mov_b32_e32 v210, v238
	v_mov_b32_e32 v211, v239
	v_lshlrev_b32_e32 v208, 16, v210
	v_and_b32_e32 v209, 0xffff0000, v210
	v_lshlrev_b32_e32 v210, 16, v211
	v_and_b32_e32 v211, 0xffff0000, v211
	v_pk_add_f32 v[142:143], v[142:143], v[208:209]
	v_pk_add_f32 v[144:145], v[144:145], v[210:211]
	v_cvt_pk_bf16_f32 v208, v142, v143
	s_nop 0
	v_cvt_pk_bf16_f32 v209, v144, v145
	s_nop 0
	global_store_dwordx2 v[192:193], v[208:209], off offset:1536
	s_waitcnt vmcnt(7)
	v_mov_b32_e32 v210, v240
	v_mov_b32_e32 v211, v241
	v_lshlrev_b32_e32 v208, 16, v210
	v_and_b32_e32 v209, 0xffff0000, v210
	v_lshlrev_b32_e32 v210, 16, v211
	v_and_b32_e32 v211, 0xffff0000, v211
	v_pk_add_f32 v[146:147], v[146:147], v[208:209]
	v_pk_add_f32 v[148:149], v[148:149], v[210:211]
	v_cvt_pk_bf16_f32 v208, v146, v147
	v_pk_mul_f32 v[218:219], v[146:147], v[146:147]
	v_cvt_pk_bf16_f32 v209, v148, v149
	v_pk_mul_f32 v[220:221], v[148:149], v[148:149]
	global_store_dwordx2 v[192:193], v[208:209], off offset:2048
	s_waitcnt vmcnt(7)
	v_mov_b32_e32 v210, v242
	v_mov_b32_e32 v211, v243
	v_lshlrev_b32_e32 v208, 16, v210
	v_and_b32_e32 v209, 0xffff0000, v210
	v_lshlrev_b32_e32 v210, 16, v211
	v_and_b32_e32 v211, 0xffff0000, v211
	v_pk_add_f32 v[150:151], v[150:151], v[208:209]
	v_pk_add_f32 v[152:153], v[152:153], v[210:211]
	v_cvt_pk_bf16_f32 v208, v150, v151
	s_nop 0
	v_cvt_pk_bf16_f32 v209, v152, v153
	s_nop 0
	global_store_dwordx2 v[192:193], v[208:209], off offset:2560
	s_waitcnt vmcnt(7)
	v_mov_b32_e32 v210, v244
	v_mov_b32_e32 v211, v245
	v_lshlrev_b32_e32 v208, 16, v210
	v_and_b32_e32 v209, 0xffff0000, v210
	v_lshlrev_b32_e32 v210, 16, v211
	v_and_b32_e32 v211, 0xffff0000, v211
	v_pk_add_f32 v[154:155], v[154:155], v[208:209]
	v_pk_add_f32 v[156:157], v[156:157], v[210:211]
	v_cvt_pk_bf16_f32 v208, v154, v155
	v_xor_b32_e32 v210, 1, v206
	v_cvt_pk_bf16_f32 v209, v156, v157
	v_cmp_lt_i32_e32 vcc, v210, v224
	v_mov_b32_e32 v211, v134
	global_store_dwordx2 v[192:193], v[208:209], off offset:3072
	v_cndmask_b32_e32 v191, v206, v210, vcc
	v_mov_b32_e32 v210, v130
	v_pk_fma_f32 v[210:211], v[210:211], v[210:211], v[212:213]
	v_pk_fma_f32 v[212:213], v[214:215], v[214:215], v[216:217]
	v_mov_b32_e32 v214, v139
	v_mov_b32_e32 v215, v141
	v_pk_add_f32 v[210:211], v[210:211], v[212:213]
	v_mov_b32_e32 v212, v138
	v_mov_b32_e32 v213, v140
	v_pk_mul_f32 v[214:215], v[214:215], v[214:215]
	v_mul_f32_e32 v216, v145, v145
	v_pk_fma_f32 v[212:213], v[212:213], v[212:213], v[214:215]
	v_mul_f32_e32 v214, v143, v143
	v_pk_add_f32 v[210:211], v[210:211], v[210:211] op_sel:[0,1] op_sel_hi:[1,0]
	v_pk_add_f32 v[212:213], v[212:213], v[212:213] op_sel:[0,1] op_sel_hi:[1,0]
	v_pk_fma_f32 v[214:215], v[142:143], v[142:143], v[214:215] op_sel_hi:[1,1,0]
	v_pk_fma_f32 v[216:217], v[144:145], v[144:145], v[216:217] op_sel_hi:[1,1,0]
	v_mov_b32_e32 v211, v218
	v_mov_b32_e32 v213, v219
	v_mov_b32_e32 v215, v220
	v_mov_b32_e32 v217, v221
	v_pk_add_f32 v[210:211], v[210:211], v[212:213]
	v_pk_add_f32 v[212:213], v[214:215], v[216:217]
	v_mov_b32_e32 v214, v151
	v_mov_b32_e32 v215, v153
	v_pk_add_f32 v[210:211], v[210:211], v[212:213]
	v_mov_b32_e32 v212, v150
	v_mov_b32_e32 v213, v152
	v_pk_mul_f32 v[214:215], v[214:215], v[214:215]
	v_pk_add_f32 v[210:211], v[210:211], v[210:211] op_sel:[0,1] op_sel_hi:[1,0]
	v_pk_fma_f32 v[212:213], v[212:213], v[212:213], v[214:215]
	v_mul_f32_e32 v214, v157, v157
	v_pk_add_f32 v[216:217], v[212:213], v[212:213] op_sel:[0,1] op_sel_hi:[1,0]
	v_mul_f32_e32 v212, v155, v155
	v_pk_fma_f32 v[208:209], v[154:155], v[154:155], v[212:213] op_sel_hi:[1,1,0]
	v_pk_fma_f32 v[218:219], v[156:157], v[156:157], v[214:215] op_sel_hi:[1,1,0]
	v_lshlrev_b32_e32 v191, 2, v191
	s_waitcnt vmcnt(7)
; #define LAS __attribute__((address_space(3)))
; __device__ __forceinline__ unsigned cvtpk(float lo, float hi) { unsigned r; asm volatile("v_cvt_pk_bf16_f32 %0, %1, %2" : "=v"(r) : "v"(lo), "v"(hi)); return r; }
; __device__ __forceinline__ unsigned cvt4_fp8(float a, float b, float c, float d) { int w = 0; w = __builtin_amdgcn_cvt_pk_fp8_f32(a, b, w, false); w = __builtin_amdgcn_cvt_pk_fp8_f32(c, d, w, true); return (unsigned)w; }
; __device__ __forceinline__ float bflo(unsigned w) { return __uint_as_float(w << 16); }
; __device__ __forceinline__ float bfhi(unsigned w) { return __uint_as_float(w & 0xffff0000u); }
; __global__ void __launch_bounds__(512, 2) mega_fwd(Args args) {
;     ...
;                   for (int j = 0; j < 8; ++j) { const u32x2 d = dr[64 * j]; nv[r][j][0] += bflo(d.x); nv[r][j][1] += bfhi(d.x); nv[r][j][2] += bflo(d.y); nv[r][j][3] += bfhi(d.y); u32x2 hw_; hw_.x = cvtpk(nv[r][j][0], nv[r][j][1]); hw_.y = cvtpk(nv[r][j][2], nv[r][j][3]); hr[64 * j] = hw_; } }
; #pragma unroll
;                 for (int j = 0; j < 8; ++j) ssq += (nv[r][j][0] * nv[r][j][0] + nv[r][j][1] * nv[r][j][1]) + (nv[r][j][2] * nv[r][j][2] + nv[r][j][3] * nv[r][j][3]);
;                 const float rstd = 1.0f / sqrtf(wave_sum(ssq) * (1.0f / DM) + EPS);
;                 unsigned* o4 = (unsigned*)(XN8 + (size_t)m * DM) + lane;
; #pragma unroll
;                 for (int j = 0; j < 8; ++j) { const f32x4 gv = ((const f32x4*)gn)[64 * j + lane]; const f32x4 y = nv[r][j] * rstd * gv;
;                     o4[64 * j] = cvt4_fp8(y[0], y[1], y[2], y[3]);
;                     u32x2 hw, lw; hw.x = cvtpk(y[0], y[1]); hw.y = cvtpk(y[2], y[3]);
;                     lw.x = cvtpk(y[0] - bflo(hw.x), y[1] - bfhi(hw.x)); lw.y = cvtpk(y[2] - bflo(hw.y), y[3] - bfhi(hw.y));
;                     *(LAS u32x2*)(Ahi + rowc * AST + (64 * j + lane) * 8) = hw; *(LAS u32x2*)(Alo + rowc * AST + (64 * j + lane) * 8) = lw; } }
	v_mov_b32_e32 v194, v246
	v_mov_b32_e32 v195, v247
	v_lshlrev_b32_e32 v212, 16, v194
	v_and_b32_e32 v213, 0xffff0000, v194
	v_lshlrev_b32_e32 v194, 16, v195
	v_and_b32_e32 v195, 0xffff0000, v195
	v_pk_add_f32 v[158:159], v[158:159], v[212:213]
	v_pk_add_f32 v[160:161], v[160:161], v[194:195]
	v_cvt_pk_bf16_f32 v194, v158, v159
	v_pk_mul_f32 v[220:221], v[158:159], v[158:159]
	v_cvt_pk_bf16_f32 v195, v160, v161
	global_store_dwordx2 v[192:193], v[194:195], off offset:3584
	global_load_dwordx4 v[212:215], v[180:181], off
	global_load_dwordx4 v[232:235], v[180:181], off offset:1024
	global_load_dwordx4 v[236:239], v[180:181], off offset:2048
	global_load_dwordx4 v[240:243], v[180:181], off offset:3072
	global_load_dwordx4 v[244:247], v[182:183], off
	global_load_dwordx4 v[248:251], v[184:185], off
	v_pk_mul_f32 v[222:223], v[160:161], v[160:161]
	v_mov_b32_e32 v211, v220
	v_mov_b32_e32 v217, v221
	v_mov_b32_e32 v209, v222
	v_mov_b32_e32 v219, v223
	v_pk_add_f32 v[192:193], v[210:211], v[216:217]
	v_pk_add_f32 v[194:195], v[208:209], v[218:219]
	v_add_u32_e32 v222, s26, v162
	v_pk_add_f32 v[192:193], v[192:193], v[194:195]
	v_xor_b32_e32 v195, 4, v206
	v_add_f32_e32 v192, v192, v193
	ds_bpermute_b32 v194, v191, v192
	v_xor_b32_e32 v193, 2, v206
	v_cmp_lt_i32_e32 vcc, v193, v224
	v_mov_b32_e32 v223, 0
	s_waitcnt lgkmcnt(0)
	v_add_f32_e32 v192, v192, v194
	v_cndmask_b32_e32 v193, v206, v193, vcc
	v_lshlrev_b32_e32 v193, 2, v193
	ds_bpermute_b32 v194, v193, v192
	v_cmp_lt_i32_e32 vcc, v195, v224
	s_waitcnt lgkmcnt(0)
	v_add_f32_e32 v192, v192, v194
	v_cndmask_b32_e32 v195, v206, v195, vcc
	v_lshlrev_b32_e32 v208, 2, v195
	ds_bpermute_b32 v194, v208, v192
	v_xor_b32_e32 v195, 8, v206
	v_cmp_lt_i32_e32 vcc, v195, v224
	s_waitcnt lgkmcnt(0)
	v_add_f32_e32 v192, v192, v194
	v_cndmask_b32_e32 v195, v206, v195, vcc
	v_lshlrev_b32_e32 v209, 2, v195
	ds_bpermute_b32 v194, v209, v192
	v_xor_b32_e32 v195, 16, v206
	v_cmp_lt_i32_e32 vcc, v195, v224
	s_waitcnt lgkmcnt(0)
	v_add_f32_e32 v192, v192, v194
	v_cndmask_b32_e32 v195, v206, v195, vcc
	v_lshlrev_b32_e32 v210, 2, v195
	ds_bpermute_b32 v194, v210, v192
	v_xor_b32_e32 v195, 32, v206
	v_cmp_lt_i32_e32 vcc, v195, v224
	v_add_u32_e32 v224, s26, v200
	s_waitcnt lgkmcnt(0)
	v_add_f32_e32 v192, v192, v194
	v_cndmask_b32_e32 v195, v206, v195, vcc
	v_lshlrev_b32_e32 v195, 2, v195
	ds_bpermute_b32 v194, v195, v192
	s_waitcnt lgkmcnt(0)
	v_add_f32_e32 v192, v192, v194
	v_fmamk_f32 v192, v192, 0x3a000000, v201
	v_mul_f32_e32 v194, 0x4f800000, v192
	v_cmp_gt_f32_e32 vcc, s54, v192
	s_nop 1
	v_cndmask_b32_e32 v192, v192, v194, vcc
	v_sqrt_f32_e32 v194, v192
	s_nop 0
	v_add_u32_e32 v195, -1, v194
	v_add_u32_e32 v211, 1, v194
	v_fma_f32 v216, -v195, v194, v192
	v_fma_f32 v217, -v211, v194, v192
	v_cmp_ge_f32_e64 s[16:17], 0, v216
	s_nop 1
	v_cndmask_b32_e64 v194, v194, v195, s[16:17]
	v_cmp_lt_f32_e64 s[16:17], 0, v217
	s_nop 1
	v_cndmask_b32_e64 v194, v194, v211, s[16:17]
	v_mul_f32_e32 v195, 0x37800000, v194
	v_cndmask_b32_e32 v194, v194, v195, vcc
	v_cmp_class_f32_e32 vcc, v192, v202
	v_mov_b32_e32 v211, 0
	s_nop 0
	v_cndmask_b32_e32 v192, v194, v192, vcc
	v_div_scale_f32 v194, s[16:17], v192, v192, 1.0
	v_rcp_f32_e32 v195, v194
	v_div_scale_f32 v216, vcc, 1.0, v192, 1.0
	s_lshl_b64 s[16:17], s[52:53], 11
	v_fma_f32 v217, -v194, v195, 1.0
	v_fmac_f32_e32 v195, v217, v195
	v_mul_f32_e32 v217, v216, v195
	v_fma_f32 v218, -v194, v217, v216
	v_fmac_f32_e32 v217, v218, v195
	v_fma_f32 v194, -v194, v217, v216
	v_div_fmas_f32 v194, v194, v195, v217
	v_div_fixup_f32 v192, v194, v192, 1.0
	v_pk_mul_f32 v[194:195], v[192:193], v[130:131] op_sel_hi:[0,1]
	s_waitcnt vmcnt(5)
	v_pk_mul_f32 v[212:213], v[194:195], v[212:213]
	v_pk_mul_f32 v[194:195], v[192:193], v[132:133] op_sel_hi:[0,1]
	v_cvt_pk_fp8_f32 v211, v212, v213
	v_pk_mul_f32 v[214:215], v[194:195], v[214:215]
	v_lshl_add_u64 v[194:195], v[172:173], 0, s[16:17]
	s_cmpk_gt_i32 s55, 0x7ff
	v_cvt_pk_fp8_f32 v211, v214, v215 op_sel:[0,0,1]
	s_cselect_b64 s[16:17], -1, 0
	s_and_b64 vcc, exec, s[16:17]
	global_store_dword v[194:195], v211, off
	v_cvt_pk_bf16_f32 v216, v212, v213
	v_cvt_pk_bf16_f32 v217, v214, v215
	s_nop 0
	v_lshlrev_b32_e32 v211, 16, v216
	v_and_b32_e32 v218, 0xffff0000, v216
	v_lshlrev_b32_e32 v219, 16, v217
	v_and_b32_e32 v220, 0xffff0000, v217
	v_sub_f32_e32 v211, v212, v211
	v_sub_f32_e32 v212, v213, v218
	v_sub_f32_e32 v213, v214, v219
	v_sub_f32_e32 v214, v215, v220
	v_cvt_pk_bf16_f32 v218, v211, v212
	v_cvt_pk_bf16_f32 v219, v213, v214
	v_pk_mul_f32 v[220:221], v[192:193], v[134:135] op_sel_hi:[0,1]
	v_mov_b32_e32 v211, 0
	s_waitcnt vmcnt(5)
	v_mov_b32_e32 v212, v232
	v_mov_b32_e32 v213, v233
	v_mov_b32_e32 v214, v234
	v_mov_b32_e32 v215, v235
	global_load_dwordx4 v[232:235], v[186:187], off
	v_pk_mul_f32 v[212:213], v[220:221], v[212:213]
	s_nop 0
	v_cvt_pk_fp8_f32 v211, v212, v213
	v_pk_mul_f32 v[220:221], v[192:193], v[136:137] op_sel_hi:[0,1]
	v_pk_mul_f32 v[214:215], v[220:221], v[214:215]
	v_add_u32_e32 v220, s27, v162
	v_cvt_pk_fp8_f32 v211, v214, v215 op_sel:[0,0,1]
	ds_write_b64 v222, v[216:217]
	ds_write_b64 v220, v[218:219]
	v_add_u32_e32 v222, s26, v167
	global_store_dword v[194:195], v211, off offset:256
	v_cvt_pk_bf16_f32 v216, v212, v213
	v_cvt_pk_bf16_f32 v217, v214, v215
	s_nop 0
	v_lshlrev_b32_e32 v211, 16, v216
	v_and_b32_e32 v218, 0xffff0000, v216
	v_lshlrev_b32_e32 v219, 16, v217
	v_and_b32_e32 v220, 0xffff0000, v217
	v_sub_f32_e32 v211, v212, v211
	v_sub_f32_e32 v212, v213, v218
	v_sub_f32_e32 v213, v214, v219
	v_sub_f32_e32 v214, v215, v220
	v_cvt_pk_bf16_f32 v218, v211, v212
	v_cvt_pk_bf16_f32 v219, v213, v214
	v_pk_mul_f32 v[220:221], v[192:193], v[138:139] op_sel_hi:[0,1]
	v_mov_b32_e32 v211, 0
	s_waitcnt vmcnt(6)
; #define LAS __attribute__((address_space(3)))
; __device__ __forceinline__ unsigned cvtpk(float lo, float hi) { unsigned r; asm volatile("v_cvt_pk_bf16_f32 %0, %1, %2" : "=v"(r) : "v"(lo), "v"(hi)); return r; }
; __device__ __forceinline__ unsigned cvt4_fp8(float a, float b, float c, float d) { int w = 0; w = __builtin_amdgcn_cvt_pk_fp8_f32(a, b, w, false); w = __builtin_amdgcn_cvt_pk_fp8_f32(c, d, w, true); return (unsigned)w; }
; __device__ __forceinline__ float bflo(unsigned w) { return __uint_as_float(w << 16); }
; __device__ __forceinline__ float bfhi(unsigned w) { return __uint_as_float(w & 0xffff0000u); }
; __global__ void __launch_bounds__(512, 2) mega_fwd(Args args) {
;     ...
;                 for (int j = 0; j < 8; ++j) { const f32x4 gv = ((const f32x4*)gn)[64 * j + lane]; const f32x4 y = nv[r][j] * rstd * gv;
;                     o4[64 * j] = cvt4_fp8(y[0], y[1], y[2], y[3]);
;                     u32x2 hw, lw; hw.x = cvtpk(y[0], y[1]); hw.y = cvtpk(y[2], y[3]);
;                     lw.x = cvtpk(y[0] - bflo(hw.x), y[1] - bfhi(hw.x)); lw.y = cvtpk(y[2] - bflo(hw.y), y[3] - bfhi(hw.y));
;                     *(LAS u32x2*)(Ahi + rowc * AST + (64 * j + lane) * 8) = hw; *(LAS u32x2*)(Alo + rowc * AST + (64 * j + lane) * 8) = lw; } }
	v_mov_b32_e32 v212, v236
	v_mov_b32_e32 v213, v237
	v_mov_b32_e32 v214, v238
	v_mov_b32_e32 v215, v239
	global_load_dwordx4 v[236:239], v[188:189], off
	v_pk_mul_f32 v[212:213], v[220:221], v[212:213]
	s_nop 0
	v_cvt_pk_fp8_f32 v211, v212, v213
	v_pk_mul_f32 v[220:221], v[192:193], v[140:141] op_sel_hi:[0,1]
	v_pk_mul_f32 v[214:215], v[220:221], v[214:215]
	v_add_u32_e32 v220, s27, v167
	v_cvt_pk_fp8_f32 v211, v214, v215 op_sel:[0,0,1]
	ds_write_b64 v222, v[216:217]
	ds_write_b64 v220, v[218:219]
	v_add_u32_e32 v222, s26, v179
	global_store_dword v[194:195], v211, off offset:512
	v_cvt_pk_bf16_f32 v216, v212, v213
	v_cvt_pk_bf16_f32 v217, v214, v215
	s_nop 0
	v_lshlrev_b32_e32 v211, 16, v216
	v_and_b32_e32 v218, 0xffff0000, v216
	v_lshlrev_b32_e32 v219, 16, v217
	v_and_b32_e32 v220, 0xffff0000, v217
	v_sub_f32_e32 v211, v212, v211
	v_sub_f32_e32 v212, v213, v218
	v_sub_f32_e32 v213, v214, v219
	v_sub_f32_e32 v214, v215, v220
	v_cvt_pk_bf16_f32 v218, v211, v212
	v_cvt_pk_bf16_f32 v219, v213, v214
	v_pk_mul_f32 v[220:221], v[192:193], v[142:143] op_sel_hi:[0,1]
	v_mov_b32_e32 v211, 0
	s_waitcnt vmcnt(7)
	v_mov_b32_e32 v212, v240
	v_mov_b32_e32 v213, v241
	v_mov_b32_e32 v214, v242
	v_mov_b32_e32 v215, v243
	v_pk_mul_f32 v[212:213], v[220:221], v[212:213]
	s_nop 0
	v_cvt_pk_fp8_f32 v211, v212, v213
	v_pk_mul_f32 v[220:221], v[192:193], v[144:145] op_sel_hi:[0,1]
	v_pk_mul_f32 v[214:215], v[220:221], v[214:215]
	v_add_u32_e32 v220, s27, v179
	v_cvt_pk_fp8_f32 v211, v214, v215 op_sel:[0,0,1]
	ds_write_b64 v222, v[216:217]
	ds_write_b64 v220, v[218:219]
	v_add_u32_e32 v222, s26, v196
	global_store_dword v[194:195], v211, off offset:768
	v_cvt_pk_bf16_f32 v216, v212, v213
	v_cvt_pk_bf16_f32 v217, v214, v215
	s_nop 0
	v_lshlrev_b32_e32 v211, 16, v216
	v_and_b32_e32 v218, 0xffff0000, v216
	v_lshlrev_b32_e32 v219, 16, v217
	v_and_b32_e32 v220, 0xffff0000, v217
	v_sub_f32_e32 v211, v212, v211
	v_sub_f32_e32 v212, v213, v218
	v_sub_f32_e32 v213, v214, v219
	v_sub_f32_e32 v214, v215, v220
	v_cvt_pk_bf16_f32 v218, v211, v212
	v_cvt_pk_bf16_f32 v219, v213, v214
	v_pk_mul_f32 v[220:221], v[192:193], v[146:147] op_sel_hi:[0,1]
	v_mov_b32_e32 v211, 0
	s_waitcnt vmcnt(7)
	v_mov_b32_e32 v212, v244
	v_mov_b32_e32 v213, v245
	v_mov_b32_e32 v214, v246
	v_mov_b32_e32 v215, v247
	v_pk_mul_f32 v[212:213], v[220:221], v[212:213]
	s_nop 0
	v_cvt_pk_fp8_f32 v211, v212, v213
	v_pk_mul_f32 v[220:221], v[192:193], v[148:149] op_sel_hi:[0,1]
	v_pk_mul_f32 v[214:215], v[220:221], v[214:215]
	v_add_u32_e32 v220, s27, v196
	v_cvt_pk_fp8_f32 v211, v214, v215 op_sel:[0,0,1]
	ds_write_b64 v222, v[216:217]
	ds_write_b64 v220, v[218:219]
	v_add_u32_e32 v222, s26, v197
	global_store_dword v[194:195], v211, off offset:1024
	v_cvt_pk_bf16_f32 v216, v212, v213
	v_cvt_pk_bf16_f32 v217, v214, v215
	s_nop 0
	v_lshlrev_b32_e32 v211, 16, v216
	v_and_b32_e32 v218, 0xffff0000, v216
	v_lshlrev_b32_e32 v219, 16, v217
	v_and_b32_e32 v220, 0xffff0000, v217
	v_sub_f32_e32 v211, v212, v211
	v_sub_f32_e32 v212, v213, v218
	v_sub_f32_e32 v213, v214, v219
	v_sub_f32_e32 v214, v215, v220
	v_cvt_pk_bf16_f32 v218, v211, v212
	v_cvt_pk_bf16_f32 v219, v213, v214
	v_pk_mul_f32 v[220:221], v[192:193], v[150:151] op_sel_hi:[0,1]
	v_mov_b32_e32 v211, 0
	s_waitcnt vmcnt(7)
	v_mov_b32_e32 v212, v248
	v_mov_b32_e32 v213, v249
	v_mov_b32_e32 v214, v250
	v_mov_b32_e32 v215, v251
	v_pk_mul_f32 v[212:213], v[220:221], v[212:213]
	s_nop 0
	v_cvt_pk_fp8_f32 v211, v212, v213
	v_pk_mul_f32 v[220:221], v[192:193], v[152:153] op_sel_hi:[0,1]
	v_pk_mul_f32 v[214:215], v[220:221], v[214:215]
	v_add_u32_e32 v220, s27, v197
	v_cvt_pk_fp8_f32 v211, v214, v215 op_sel:[0,0,1]
	ds_write_b64 v222, v[216:217]
	ds_write_b64 v220, v[218:219]
	v_add_u32_e32 v222, s26, v198
	global_store_dword v[194:195], v211, off offset:1280
	v_cvt_pk_bf16_f32 v216, v212, v213
	v_cvt_pk_bf16_f32 v217, v214, v215
	s_nop 0
	v_lshlrev_b32_e32 v211, 16, v216
	v_and_b32_e32 v218, 0xffff0000, v216
	v_lshlrev_b32_e32 v219, 16, v217
	v_and_b32_e32 v220, 0xffff0000, v217
	v_sub_f32_e32 v211, v212, v211
	v_sub_f32_e32 v212, v213, v218
	v_sub_f32_e32 v213, v214, v219
	v_sub_f32_e32 v214, v215, v220
	v_cvt_pk_bf16_f32 v218, v211, v212
	v_cvt_pk_bf16_f32 v219, v213, v214
	v_pk_mul_f32 v[220:221], v[192:193], v[154:155] op_sel_hi:[0,1]
	v_mov_b32_e32 v211, 0
	s_waitcnt vmcnt(6)
	v_mov_b32_e32 v212, v232
	v_mov_b32_e32 v213, v233
	v_mov_b32_e32 v214, v234
	v_mov_b32_e32 v215, v235
	v_pk_mul_f32 v[212:213], v[220:221], v[212:213]
	s_nop 0
	v_cvt_pk_fp8_f32 v211, v212, v213
	v_pk_mul_f32 v[220:221], v[192:193], v[156:157] op_sel_hi:[0,1]
	v_pk_mul_f32 v[214:215], v[220:221], v[214:215]
	v_add_u32_e32 v220, s27, v198
	v_cvt_pk_fp8_f32 v211, v214, v215 op_sel:[0,0,1]
	ds_write_b64 v222, v[216:217]
	ds_write_b64 v220, v[218:219]
	v_add_u32_e32 v222, s27, v199
	global_store_dword v[194:195], v211, off offset:1536
	v_cvt_pk_bf16_f32 v216, v212, v213
	v_cvt_pk_bf16_f32 v217, v214, v215
	s_nop 0
	v_lshlrev_b32_e32 v211, 16, v216
	v_and_b32_e32 v218, 0xffff0000, v216
	v_lshlrev_b32_e32 v219, 16, v217
	v_and_b32_e32 v220, 0xffff0000, v217
	v_sub_f32_e32 v211, v212, v211
	v_sub_f32_e32 v212, v213, v218
	v_sub_f32_e32 v213, v214, v219
	v_sub_f32_e32 v214, v215, v220
	v_cvt_pk_bf16_f32 v218, v211, v212
	v_cvt_pk_bf16_f32 v219, v213, v214
	v_pk_mul_f32 v[220:221], v[192:193], v[158:159] op_sel_hi:[0,1]
	v_add_u32_e32 v211, s26, v199
	ds_write_b64 v211, v[216:217]
	ds_write_b64 v222, v[218:219]
	s_waitcnt vmcnt(5)
	v_mov_b32_e32 v212, v236
	v_mov_b32_e32 v213, v237
	v_mov_b32_e32 v214, v238
	v_mov_b32_e32 v215, v239
	v_pk_mul_f32 v[212:213], v[220:221], v[212:213]
	s_nop 0
	v_cvt_pk_fp8_f32 v223, v212, v213
	v_pk_mul_f32 v[220:221], v[192:193], v[160:161] op_sel_hi:[0,1]
	v_pk_mul_f32 v[214:215], v[220:221], v[214:215]
	s_nop 0
	v_cvt_pk_fp8_f32 v223, v214, v215 op_sel:[0,0,1]
	global_store_dword v[194:195], v223, off offset:1792
	v_cvt_pk_bf16_f32 v194, v212, v213
	v_cvt_pk_bf16_f32 v195, v214, v215
	s_nop 0
	v_and_b32_e32 v211, 0xffff0000, v194
	v_lshlrev_b32_e32 v216, 16, v195
	v_lshlrev_b32_e32 v192, 16, v194
	v_and_b32_e32 v217, 0xffff0000, v195
	v_sub_f32_e32 v211, v213, v211
	v_sub_f32_e32 v213, v214, v216
	v_sub_f32_e32 v192, v212, v192
	v_sub_f32_e32 v214, v215, v217
	v_cvt_pk_bf16_f32 v212, v192, v211
	v_cvt_pk_bf16_f32 v213, v213, v214
	ds_write_b64 v224, v[194:195]
	ds_write_b64 v225, v[212:213]
	s_cbranch_vccnz .LBB0_1998
; __device__ __forceinline__ unsigned cvtpk(float lo, float hi) { unsigned r; asm volatile("v_cvt_pk_bf16_f32 %0, %1, %2" : "=v"(r) : "v"(lo), "v"(hi)); return r; }
; __device__ __forceinline__ float bflo(unsigned w) { return __uint_as_float(w << 16); }
; __device__ __forceinline__ float bfhi(unsigned w) { return __uint_as_float(w & 0xffff0000u); }
; __global__ void __launch_bounds__(512, 2) mega_fwd(Args args) {
;     ...
;                 { const u32x2* dr = (const u32x2*)(D7 + (size_t)m * DM) + lane; u32x2* hr = (u32x2*)(H1 + (size_t)m * DM) + lane;
; #pragma unroll
;                   for (int j = 0; j < 8; ++j) { const u32x2 d = dr[64 * j]; nv[r][j][0] += bflo(d.x); nv[r][j][1] += bfhi(d.x); nv[r][j][2] += bflo(d.y); nv[r][j][3] += bfhi(d.y); u32x2 hw_; hw_.x = cvtpk(nv[r][j][0], nv[r][j][1]); hw_.y = cvtpk(nv[r][j][2], nv[r][j][3]); hr[64 * j] = hw_; } }
;     ...
;             if (ch + G < T / CR) {
; #pragma unroll
;                 for (int r = 0; r < RPW; ++r) { const f32x4* xr = (const f32x4*)(x + (size_t)((ch + G) * CR + wave * RPW + r) * DM) + lane;
; #pragma unroll
;                     for (int j = 0; j < 8; ++j) nv[r][j] = xr[64 * j]; } }
	s_add_i32 s52, s41, s3
	s_ashr_i32 s53, s52, 31
	s_lshl_b64 s[52:53], s[52:53], 13
	v_lshl_add_u64 v[146:147], v[174:175], 0, s[52:53]
	v_add_co_u32_e32 v158, vcc, 0x1000, v146
	global_load_dwordx4 v[130:133], v[146:147], off
	global_load_dwordx4 v[134:137], v[146:147], off offset:1024
	global_load_dwordx4 v[138:141], v[146:147], off offset:2048
	global_load_dwordx4 v[142:145], v[146:147], off offset:3072
	v_addc_co_u32_e32 v159, vcc, 0, v147, vcc
	global_load_dwordx4 v[146:149], v[158:159], off
	global_load_dwordx4 v[150:153], v[158:159], off offset:1024
	global_load_dwordx4 v[154:157], v[158:159], off offset:2048
	s_nop 0
	global_load_dwordx4 v[158:161], v[158:159], off offset:3072
	s_add_i32 s98, s74, s3
	s_add_i32 s98, s98, s40
	s_ashr_i32 s99, s98, 31
	s_lshl_b64 s[98:99], s[98:99], 12
	v_lshl_add_u64 v[248:249], v[168:169], 0, s[98:99]
	global_load_dwordx2 v[232:233], v[248:249], off
	global_load_dwordx2 v[234:235], v[248:249], off offset:512
	global_load_dwordx2 v[236:237], v[248:249], off offset:1024
	global_load_dwordx2 v[238:239], v[248:249], off offset:1536
	global_load_dwordx2 v[240:241], v[248:249], off offset:2048
	global_load_dwordx2 v[242:243], v[248:249], off offset:2560
	global_load_dwordx2 v[244:245], v[248:249], off offset:3072
	global_load_dwordx2 v[246:247], v[248:249], off offset:3584

; __global__ void __launch_bounds__(512, 2) mega_fwd(Args args) {
;     extern __shared__ __attribute__((aligned(16))) unsigned char lds_raw[];
	.amdhsa_kernel _Z8mega_fwd4Args
		.amdhsa_group_segment_fixed_size 0
		.amdhsa_private_segment_fixed_size 0
		.amdhsa_kernarg_size 480
		.amdhsa_user_sgpr_count 2
		.amdhsa_user_sgpr_dispatch_ptr 0
		.amdhsa_user_sgpr_queue_ptr 0
		.amdhsa_user_sgpr_kernarg_segment_ptr 1
		.amdhsa_user_sgpr_dispatch_id 0
		.amdhsa_user_sgpr_kernarg_preload_length 0
		.amdhsa_user_sgpr_kernarg_preload_offset 0
		.amdhsa_user_sgpr_private_segment_size 0
		.amdhsa_uses_dynamic_stack 0
		.amdhsa_enable_private_segment 0
		.amdhsa_system_sgpr_workgroup_id_x 1
		.amdhsa_system_sgpr_workgroup_id_y 0
		.amdhsa_system_sgpr_workgroup_id_z 0
		.amdhsa_system_sgpr_workgroup_info 0
		.amdhsa_system_vgpr_workitem_id 0
		.amdhsa_next_free_vgpr 253
		.amdhsa_next_free_sgpr 102
		.amdhsa_accum_offset 256
		.amdhsa_reserve_vcc 1
		.amdhsa_float_round_mode_32 0
		.amdhsa_float_round_mode_16_64 0
		.amdhsa_float_denorm_mode_32 3
		.amdhsa_float_denorm_mode_16_64 3
		.amdhsa_dx10_clamp 1
		.amdhsa_ieee_mode 1
		.amdhsa_fp16_overflow 0
		.amdhsa_tg_split 0
		.amdhsa_exception_fp_ieee_invalid_op 0
		.amdhsa_exception_fp_denorm_src 0
		.amdhsa_exception_fp_ieee_div_zero 0
		.amdhsa_exception_fp_ieee_overflow 0
		.amdhsa_exception_fp_ieee_underflow 0
		.amdhsa_exception_fp_ieee_inexact 0
		.amdhsa_exception_int_div_zero 0
	.end_amdhsa_kernel

; __global__ void __launch_bounds__(512, 2) mega_fwd(Args args) {
;     extern __shared__ __attribute__((aligned(16))) unsigned char lds_raw[];
amdhsa.kernels:
  - .agpr_count:     0
    .args:
      - .offset:         0
        .size:           224
        .value_kind:     by_value
      - .offset:         224
        .size:           4
        .value_kind:     hidden_block_count_x
      - .offset:         228
        .size:           4
        .value_kind:     hidden_block_count_y
      - .offset:         232
        .size:           4
        .value_kind:     hidden_block_count_z
      - .offset:         236
        .size:           2
        .value_kind:     hidden_group_size_x
      - .offset:         238
        .size:           2
        .value_kind:     hidden_group_size_y
      - .offset:         240
        .size:           2
        .value_kind:     hidden_group_size_z
      - .offset:         242
        .size:           2
        .value_kind:     hidden_remainder_x
      - .offset:         244
        .size:           2
        .value_kind:     hidden_remainder_y
      - .offset:         246
        .size:           2
        .value_kind:     hidden_remainder_z
      - .offset:         264
        .size:           8
        .value_kind:     hidden_global_offset_x
      - .offset:         272
        .size:           8
        .value_kind:     hidden_global_offset_y
      - .offset:         280
        .size:           8
        .value_kind:     hidden_global_offset_z
      - .offset:         288
        .size:           2
        .value_kind:     hidden_grid_dims
      - .offset:         344
        .size:           4
        .value_kind:     hidden_dynamic_lds_size
    .group_segment_fixed_size: 0
    .kernarg_segment_align: 8
    .kernarg_segment_size: 480
    .language:       OpenCL C
    .language_version:
      - 2
      - 0
    .max_flat_workgroup_size: 512
    .name:           _Z8mega_fwd4Args
    .private_segment_fixed_size: 0
    .sgpr_count:     108
    .sgpr_spill_count: 6
    .symbol:         _Z8mega_fwd4Args.kd
    .uniform_work_group_size: 1
    .uses_dynamic_stack: false
    .vgpr_count:     253
    .vgpr_spill_count: 0
    .wavefront_size: 64
